# v27 + in_proj GEMM: per-workgroup rotation of the K-tile order (4 classes) to spread L2 channel load
# speedup vs baseline: 1.0133x; 1.0133x over previous
; #define PG8_WAIT_V(n) asm volatile("s_waitcnt vmcnt(" #n ")" ::: "memory")
; #define PG8_BAR __builtin_amdgcn_s_barrier()
;     ...
;     for (int i = 0; i < 2; ++i) { int R, C; stage_rc(tid * 16 + i * 8192, R, C);
;         const int Rb = Epi::COL16 ? (64 * (R >> 5) + 16 * ((R & 15) >> 2) + 4 * ((R >> 4) & 1) + (R & 3)) : ((R & ~31) + perm32(R & 31));
;         voffB[i] = (unsigned)(Rb * K + C) * 2u; }
;     constexpr size_t kstep = (size_t)(BK * 2);
;     constexpr size_t hstep = (size_t)HALF * K * 2;
;     constexpr size_t bstep = Epi::COL16 ? (size_t)8 * K * 2 : hstep;
;     const unsigned ldsw = (unsigned)wid * 1024u;
;     const int aoff = lds_byte(wr * 64 + fr, fq * 8), boff = lds_byte(wc * 32 + fr, fq * 8);
;     ...
;     Unit cur, nxt; int ui = 0;
;     if (!S.next(0, cur)) return;
;     f32x4 acc[2][2][4][2];
; #pragma unroll
;     for (int a = 0; a < 2; ++a)
; #pragma unroll
;         for (int b = 0; b < 2; ++b)
; #pragma unroll
;             for (int m = 0; m < 4; ++m)
; #pragma unroll
;                 for (int n = 0; n < 2; ++n) acc[a][b][m][n] = (f32x4){0.f, 0.f, 0.f, 0.f};
;     bf16x8 At[4][2], B0[2][2], B1[2][2];
;     int scw_ = Epi::SC_W, scx_ = Epi::SC_X; asm volatile("" : "+v"(scw_), "+v"(scx_));
;     constexpr bool GATHER = Sched::GATHER;
;     constexpr size_t ah = GATHER ? 0 : hstep;
;     unsigned va[2][2], vn[2][2];
;     S.a_voff(cur, va);
;     ...
;     const char* cA = S.a_base(cur); const char* cB = S.b_base(cur);
;     if constexpr (SP2) {
;         PG8_STAGE(PG8_SB(0, 0), cB, voffB); PG8_STAGE(PG8_SB(0, 1), cB + bstep, voffB); PG8_STAGE(PG8_SA(0, 0), cA, va[0]); PG8_STAGE(PG8_SA(0, 1), cA + ah, VA1);
;         if (wr == 1) PG8_BAR;
;         PG8_WAIT_V(2); PG8_BAR;
;         PG8_STAGE(PG8_SB(1, 0), cB + kstep, voffB); PG8_STAGE(PG8_SA(1, 0), cA + kstep, va[0]); PG8_STAGE(PG8_SB(1, 1), cB + bstep + kstep, voffB);
;         PG8_WAIT_V(6); PG8_BAR;
;     } else {
;         PG8_STAGE(PG8_SB(0, 0), cB, voffB); PG8_STAGE(PG8_SA(0, 0), cA, va[0]); PG8_STAGE(PG8_SB(0, 1), cB + bstep, voffB); PG8_STAGE(PG8_SA(0, 1), cA + ah, VA1);
;         if (wr == 1) PG8_BAR;
;         PG8_WAIT_V(4); PG8_BAR;
;         PG8_STAGE(PG8_SB(1, 0), cB + kstep, voffB); PG8_STAGE(PG8_SA(1, 0), cA + kstep, va[0]); PG8_STAGE(PG8_SB(1, 1), cB + bstep + kstep, voffB);
;         PG8_WAIT_V(6); PG8_BAR;
.LBB0_187:
	v_mov_b32_e32 v10, v0
	s_mov_b64 s[4:5], s[0:1]
	s_load_dword s36, s[22:23], 0x0
	s_cmpk_gt_i32 s2, 0x9ff
	v_readfirstlane_b32 s15, v10
	s_cbranch_scc1 .LBB0_203
	s_bfe_u32 s69, s2, 0x20004
	s_lshl_b32 s99, s69, 1
	s_sub_i32 s99, 4, s99
	s_lshl_b32 s69, s69, 8
	v_lshlrev_b32_e32 v1, 4, v10
	v_add_u32_e32 v2, 0x2000, v1
	v_ashrrev_i32_e32 v3, 31, v2
	v_lshrrev_b32_e32 v3, 22, v3
	v_add_u32_e32 v3, v2, v3
	v_ashrrev_i32_e32 v11, 10, v3
	v_mul_i32_i24_e32 v3, 0x400, v11
	v_sub_u32_e32 v2, v2, v3
	v_lshrrev_b32_e32 v3, 4, v2
	v_bitop3_b32 v2, v3, v2, 32 bitop3:0x6c
	v_ashrrev_i32_e32 v3, 31, v2
	v_lshrrev_b32_e32 v3, 26, v3
	v_add_u32_e32 v3, v2, v3
	v_lshlrev_b32_e32 v4, 3, v11
	v_ashrrev_i32_e32 v12, 6, v3
	v_and_b32_e32 v5, -16, v4
	v_add_u32_e32 v5, v12, v5
	v_and_b32_e32 v6, 3, v12
	s_mov_b32 s8, 0x3fffe0
	v_and_or_b32 v6, v5, s8, v6
	v_lshrrev_b32_e32 v7, 2, v5
	v_lshlrev_b32_e32 v5, 1, v5
	v_and_b32_e32 v3, 0xc0, v3
	v_and_b32_e32 v7, 4, v7
	v_and_b32_e32 v5, 24, v5
	v_sub_u32_e32 v2, v2, v3
	v_mov_b32_e32 v3, 1
	v_or3_b32 v5, v6, v7, v5
	v_lshlrev_b32_e32 v6, 5, v11
	v_ashrrev_i16_sdwa v2, v3, sext(v2) dst_sel:DWORD dst_unused:UNUSED_PAD src0_sel:DWORD src1_sel:BYTE_0
	v_and_b32_e32 v6, 32, v6
	v_bfe_i32 v13, v2, 0, 16
	v_add_lshl_u32 v2, v6, v13, 1
	v_lshl_add_u32 v162, v5, 10, v2
	v_bfe_i32 v5, v10, 27, 1
	s_load_dwordx2 s[4:5], s[4:5], 0xc0
	v_lshrrev_b32_e32 v5, 22, v5
	v_add_u32_e32 v5, v1, v5
	v_and_b32_e32 v5, 0xfffffc00, v5
	v_sub_u32_e32 v1, v1, v5
	v_lshrrev_b32_e32 v5, 4, v1
	v_ashrrev_i32_e32 v6, 31, v10
	s_waitcnt lgkmcnt(0)
	s_add_u32 s37, s4, 0xd1c0000
	v_bitop3_b32 v1, v5, v1, 32 bitop3:0x6c
	v_lshrrev_b32_e32 v6, 26, v6
	s_addc_u32 s38, s5, 0
	v_ashrrev_i32_e32 v5, 31, v1
	v_add_u32_e32 v6, v10, v6
	s_add_u32 s39, s4, 0x100000
	v_lshrrev_b32_e32 v5, 26, v5
	v_ashrrev_i32_e32 v15, 6, v6
	s_addc_u32 s41, s5, 0
	s_ashr_i32 s12, s15, 6
	v_add_u32_e32 v5, v1, v5
	v_lshlrev_b32_e32 v6, 3, v15
	s_ashr_i32 s18, s15, 8
	s_lshl_b32 s42, s12, 10
	v_ashrrev_i32_e32 v14, 6, v5
	v_and_b32_e32 v7, -16, v6
	s_cmp_lt_i32 s33, 0
	v_add_u32_e32 v7, v14, v7
	v_and_b32_e32 v8, 3, v14
	s_movk_i32 s43, 0x141
	v_and_or_b32 v8, v7, s8, v8
	s_cselect_b32 s8, s43, 0x140
	s_mul_i32 s8, s33, s8
	s_add_i32 s8, s8, s3
	s_mul_hi_i32 s9, s8, 0x66666667
	s_lshr_b32 s10, s9, 31
	s_ashr_i32 s9, s9, 5
	s_add_i32 s9, s9, s10
	s_lshl_b32 s10, s9, 3
	s_mulk_i32 s9, 0x50
	s_sub_i32 s8, s8, s9
	s_bfe_i32 s9, s8, 0x80000
	s_bfe_u32 s9, s9, 0x3000c
	s_add_i32 s9, s8, s9
	s_bfe_i32 s11, s9, 0x80000
	s_and_b32 s9, s9, 0xf8
	s_sub_i32 s8, s8, s9
	s_sext_i32_i16 s11, s11
	s_sext_i32_i8 s8, s8
	v_lshrrev_b32_e32 v9, 2, v7
	v_lshlrev_b32_e32 v7, 1, v7
	v_and_b32_e32 v5, 0xc0, v5
	s_lshr_b32 s14, s11, 3
	s_add_i32 s16, s10, s8
	v_and_b32_e32 v9, 4, v9
	v_and_b32_e32 v7, 24, v7
	v_sub_u32_e32 v1, v1, v5
	s_ashr_i32 s17, s16, 31
	s_bfe_i64 s[10:11], s[14:15], 0x100000
	v_or3_b32 v7, v8, v9, v7
	v_lshlrev_b32_e32 v8, 5, v15
	v_ashrrev_i16_sdwa v1, v3, sext(v1) dst_sel:DWORD dst_unused:UNUSED_PAD src0_sel:DWORD src1_sel:BYTE_0
	s_lshl_b64 s[8:9], s[16:17], 18
	s_lshl_b64 s[10:11], s[10:11], 18
	v_and_b32_e32 v8, 32, v8
	v_bfe_i32 v16, v1, 0, 16
	s_add_u32 s30, s39, s10
	v_add_lshl_u32 v3, v8, v16, 1
	s_addc_u32 s31, s41, s11
	s_add_u32 s30, s30, s69
	s_addc_u32 s31, s31, 0
	s_add_i32 s17, s42, 0
	v_lshl_add_u32 v164, v7, 10, v3
	v_mov_b32_e32 v1, 0x79797979
	v_mov_b32_e32 v186, 0x7f7f7f7f
	s_add_i32 m0, s17, 0x10000
	v_and_b32_e32 v5, 0x3ffff0, v6
	global_load_lds_dwordx4 v164, s[30:31]
	s_add_i32 m0, s17, 0x12000
	s_add_u32 s10, s30, 0x20000
	global_load_lds_dwordx4 v162, s[30:31]
	s_addc_u32 s11, s31, 0
	s_add_i32 m0, s17, 0x14000
	v_add_u32_e32 v5, v14, v5
	global_load_lds_dwordx4 v164, s[10:11]
	s_add_i32 m0, s17, 0x16000
	s_add_u32 s28, s37, s8
	v_lshl_add_u32 v166, v5, 10, v3
	v_and_b32_e32 v3, 0x3ffff0, v4
	s_addc_u32 s29, s38, s9
	s_add_u32 s28, s28, s69
	s_addc_u32 s29, s29, 0
	s_add_i32 s44, s17, 0x2000
	v_add_u32_e32 v3, v12, v3
	global_load_lds_dwordx4 v162, s[10:11]
	s_mov_b32 m0, s17
	s_add_u32 s8, s28, 0x20000
	v_lshl_add_u32 v168, v3, 10, v2
	global_load_lds_dwordx4 v166, s[28:29]
	s_mov_b32 m0, s44
	s_addc_u32 s9, s29, 0
	s_add_i32 s45, s17, 0x4000
	global_load_lds_dwordx4 v168, s[28:29]
	s_mov_b32 m0, s45
	s_add_i32 s46, s17, 0x6000
	global_load_lds_dwordx4 v166, s[8:9]
	s_mov_b32 m0, s46
	v_mov_b32_e32 v165, 0
	global_load_lds_dwordx4 v168, s[8:9]
	v_mov_b32_e32 v163, v165
	v_mov_b32_e32 v167, v165
	v_mov_b32_e32 v169, v165
	s_cmp_eq_u32 s18, 1
	s_mov_b32 s47, 0
	v_lshl_add_u64 v[8:9], s[30:31], 0, v[164:165]
	v_lshl_add_u64 v[6:7], s[30:31], 0, v[162:163]
	v_lshl_add_u64 v[2:3], s[28:29], 0, v[166:167]
	s_cselect_b64 s[8:9], -1, 0
	s_cmp_lg_u32 s18, 1
	v_lshl_add_u64 v[4:5], s[28:29], 0, v[168:169]
	s_cbranch_scc1 .LBB0_190
	s_barrier

; #define PG8_STAGE(bufoff, gbase, voff) do { _Pragma("unroll") for (int _i = 0; _i < 2; ++_i) \
;         __builtin_amdgcn_global_load_lds((const unsigned*)((const char*)(gbase) + (voff)[_i]), (LAS unsigned*)(lds + (bufoff) + ldsw + _i * 8192), 16, 0, 0); } while (0)
; #define PG8_LDA(dst, b, h) do { _Pragma("unroll") for (int m = 0; m < 4; ++m) _Pragma("unroll") for (int k = 0; k < 2; ++k) dst[m][k] = *(const LAS bf16x8*)(lds + PG8_SA(b, h) + aoff + m * 2048 + k * 1024); } while (0)
; #define PG8_WAIT_V(n) asm volatile("s_waitcnt vmcnt(" #n ")" ::: "memory")
; #define PG8_BAR __builtin_amdgcn_s_barrier()
;     ...
;         const bool has_next = S.next(ui + 1, nxt);
;         const char* nA = has_next ? S.a_base(nxt) : cA; const char* nB = has_next ? S.b_base(nxt) : cB;
;         const bool full = cur.nv > 128;
;         if constexpr (GATHER) { if (has_next) S.a_voff(nxt, vn); else { vn[0][0] = va[0][0]; vn[0][1] = va[0][1]; vn[1][0] = va[1][0]; vn[1][1] = va[1][1]; } }
; #pragma unroll 1
;         for (int t = 0; t < nt; t += 2) {
;             const bool last = (t == nt - 2);
;             const char* a1 = cA + (size_t)(t + 1) * kstep;
;             const char* a2 = last ? nA : cA + (size_t)(t + 2) * kstep; const char* b2 = last ? nB : cB + (size_t)(t + 2) * kstep;
;             const char* a3 = a2 + kstep; const char* b3 = b2 + kstep;
;             unsigned v2[2][2];
;             if constexpr (GATHER) { v2[0][0] = last ? vn[0][0] : va[0][0]; v2[0][1] = last ? vn[0][1] : va[0][1]; v2[1][0] = last ? vn[1][0] : va[1][0]; v2[1][1] = last ? vn[1][1] : va[1][1]; }
;             else { v2[0][0] = va[0][0]; v2[0][1] = va[0][1]; v2[1][0] = va[0][0]; v2[1][1] = va[0][1]; }
;             if constexpr (SP2) {
;             PG8_LDB(B0, 0, 0); PG8_LDB(B1, 0, 1); PG8_SCHED; PG8_LDA(At, 0, 0); PG8_STAGE(PG8_SA(1, 1), a1 + ah, VA1);
;             PG8_WAIT_V(8); PG8_WAIT_L(0); PG8_BAR; PG8_MMA(0, 0, At, B0); PG8_MMA(0, 1, At, B1); PG8_BAR; PG8_SCHED;
;             PG8_LDA(At, 0, 1); PG8_STAGE(PG8_SB(0, 0), b2, voffB); PG8_STAGE(PG8_SB(0, 1), b2 + bstep, voffB); PG8_STAGE(PG8_SA(0, 0), a2, v2[0]);
;     ...
;         for (int a = 0; a < 2; ++a)
; #pragma unroll
;             for (int b = 0; b < 2; ++b)
; #pragma unroll
;                 for (int m = 0; m < 4; ++m)
; #pragma unroll
;                     for (int n = 0; n < 2; ++n) acc[a][b][m][n] = (f32x4){0.f, 0.f, 0.f, 0.f};
.LBB0_195:
	s_ashr_i32 s23, s22, 31
	s_lshl_b64 s[24:25], s[22:23], 18
	s_add_u32 s24, s37, s24
	s_addc_u32 s25, s38, s25
	s_add_u32 s24, s24, s69
	s_addc_u32 s25, s25, 0
	s_and_b64 s[26:27], s[4:5], exec
	s_cselect_b32 s23, s25, s29
	s_cselect_b32 s55, s24, s28
	s_ashr_i32 s19, s18, 31
	s_lshl_b64 s[26:27], s[18:19], 18
	s_add_u32 s26, s39, s26
	s_addc_u32 s27, s41, s27
	s_add_u32 s26, s26, s69
	s_addc_u32 s27, s27, 0
	s_and_b64 s[34:35], s[4:5], exec
	s_cselect_b32 s19, s27, s31
	s_cselect_b32 s56, s26, s30
	s_add_u32 s28, s28, 0x20080
	s_addc_u32 s29, s29, 0
	s_add_u32 s58, s30, 0x100
	v_mov_b32_e32 v34, 0
	s_addc_u32 s59, s31, 0
	s_cmp_eq_u32 s99, -2
	s_cbranch_scc0 .Lkr_a
	s_sub_u32 s58, s58, 0x400
	s_subb_u32 s59, s59, 0
.Lkr_a:
	s_mov_b32 s64, -2
	v_mov_b32_e32 v35, v34
	v_mov_b32_e32 v36, v34
	v_mov_b32_e32 v37, v34
	v_mov_b32_e32 v38, v34
	v_mov_b32_e32 v39, v34
	v_mov_b32_e32 v40, v34
	v_mov_b32_e32 v41, v34
	v_mov_b32_e32 v42, v34
	v_mov_b32_e32 v43, v34
	v_mov_b32_e32 v44, v34
	v_mov_b32_e32 v45, v34
	v_mov_b32_e32 v46, v34
	v_mov_b32_e32 v47, v34
	v_mov_b32_e32 v48, v34
	v_mov_b32_e32 v49, v34
	v_mov_b32_e32 v50, v34
	v_mov_b32_e32 v51, v34
	v_mov_b32_e32 v52, v34
	v_mov_b32_e32 v53, v34
	v_mov_b32_e32 v54, v34
	v_mov_b32_e32 v55, v34
	v_mov_b32_e32 v56, v34
	v_mov_b32_e32 v57, v34
	v_mov_b32_e32 v58, v34
	v_mov_b32_e32 v59, v34
	v_mov_b32_e32 v60, v34
	v_mov_b32_e32 v61, v34
	v_mov_b32_e32 v62, v34
	v_mov_b32_e32 v63, v34
	v_mov_b32_e32 v64, v34
	v_mov_b32_e32 v65, v34
	v_mov_b32_e32 v66, v34
	v_mov_b32_e32 v67, v34
	v_mov_b32_e32 v68, v34
	v_mov_b32_e32 v69, v34
	v_mov_b32_e32 v74, v34
	v_mov_b32_e32 v75, v34
	v_mov_b32_e32 v76, v34
	v_mov_b32_e32 v77, v34
	v_mov_b32_e32 v90, v34
	v_mov_b32_e32 v91, v34
	v_mov_b32_e32 v92, v34
	v_mov_b32_e32 v93, v34
	v_mov_b32_e32 v102, v34
	v_mov_b32_e32 v103, v34
	v_mov_b32_e32 v104, v34
	v_mov_b32_e32 v105, v34
	v_mov_b32_e32 v122, v34
	v_mov_b32_e32 v123, v34
	v_mov_b32_e32 v124, v34
	v_mov_b32_e32 v125, v34
	v_mov_b32_e32 v126, v34
	v_mov_b32_e32 v127, v34
	v_mov_b32_e32 v128, v34
	v_mov_b32_e32 v129, v34
	v_mov_b32_e32 v138, v34
	v_mov_b32_e32 v139, v34
	v_mov_b32_e32 v140, v34
	v_mov_b32_e32 v141, v34
	v_mov_b32_e32 v142, v34
	v_mov_b32_e32 v143, v34
	v_mov_b32_e32 v144, v34
	v_mov_b32_e32 v145, v34
	v_mov_b32_e32 v106, v34
	v_mov_b32_e32 v107, v34
	v_mov_b32_e32 v108, v34
	v_mov_b32_e32 v109, v34
	v_mov_b32_e32 v118, v34
	v_mov_b32_e32 v119, v34
	v_mov_b32_e32 v120, v34
	v_mov_b32_e32 v121, v34
	v_mov_b32_e32 v130, v34
	v_mov_b32_e32 v131, v34
	v_mov_b32_e32 v132, v34
	v_mov_b32_e32 v133, v34
	v_mov_b32_e32 v134, v34
	v_mov_b32_e32 v135, v34
	v_mov_b32_e32 v136, v34
	v_mov_b32_e32 v137, v34
	v_mov_b32_e32 v146, v34
	v_mov_b32_e32 v147, v34
	v_mov_b32_e32 v148, v34
	v_mov_b32_e32 v149, v34
	v_mov_b32_e32 v150, v34
	v_mov_b32_e32 v151, v34
	v_mov_b32_e32 v152, v34
	v_mov_b32_e32 v153, v34
	v_mov_b32_e32 v154, v34
	v_mov_b32_e32 v155, v34
	v_mov_b32_e32 v156, v34
	v_mov_b32_e32 v157, v34
	v_mov_b32_e32 v158, v34
	v_mov_b32_e32 v159, v34
	v_mov_b32_e32 v160, v34
	v_mov_b32_e32 v161, v34
	v_mov_b32_e32 v110, v34
	v_mov_b32_e32 v111, v34
	v_mov_b32_e32 v112, v34
	v_mov_b32_e32 v113, v34
	v_mov_b32_e32 v114, v34
	v_mov_b32_e32 v115, v34
	v_mov_b32_e32 v116, v34
	v_mov_b32_e32 v117, v34
	v_mov_b32_e32 v94, v34
	v_mov_b32_e32 v95, v34
	v_mov_b32_e32 v96, v34
	v_mov_b32_e32 v97, v34
	v_mov_b32_e32 v98, v34
	v_mov_b32_e32 v99, v34
	v_mov_b32_e32 v100, v34
	v_mov_b32_e32 v101, v34
	v_mov_b32_e32 v82, v34
	v_mov_b32_e32 v83, v34
	v_mov_b32_e32 v84, v34
	v_mov_b32_e32 v85, v34
	v_mov_b32_e32 v86, v34
	v_mov_b32_e32 v87, v34
	v_mov_b32_e32 v88, v34
	v_mov_b32_e32 v89, v34
	v_mov_b32_e32 v70, v34
	v_mov_b32_e32 v71, v34
	v_mov_b32_e32 v72, v34
	v_mov_b32_e32 v73, v34
	v_mov_b32_e32 v78, v34
	v_mov_b32_e32 v79, v34
	v_mov_b32_e32 v80, v34
	v_mov_b32_e32 v81, v34
.LBB0_196:
	ds_read_b128 v[26:29], v190
	ds_read_b128 v[30:33], v190 offset:1024
	ds_read_b128 v[18:21], v190 offset:2048
	ds_read_b128 v[22:25], v190 offset:3072
	ds_read_b128 v[10:13], v191
	ds_read_b128 v[14:17], v191 offset:1024
	ds_read_b128 v[2:5], v191 offset:2048
	ds_read_b128 v[6:9], v191 offset:3072
	s_add_u32 s30, s28, 0xfffe0080
	s_addc_u32 s31, s29, -1
	s_cmp_eq_u32 s64, s99
	s_cbranch_scc0 .Lkr_b
	s_sub_u32 s30, s30, 0x400
	s_subb_u32 s31, s31, 0
; #define PG8_STAGE(bufoff, gbase, voff) do { _Pragma("unroll") for (int _i = 0; _i < 2; ++_i) \
;         __builtin_amdgcn_global_load_lds((const unsigned*)((const char*)(gbase) + (voff)[_i]), (LAS unsigned*)(lds + (bufoff) + ldsw + _i * 8192), 16, 0, 0); } while (0)
; #define PG8_LDA(dst, b, h) do { _Pragma("unroll") for (int m = 0; m < 4; ++m) _Pragma("unroll") for (int k = 0; k < 2; ++k) dst[m][k] = *(const LAS bf16x8*)(lds + PG8_SA(b, h) + aoff + m * 2048 + k * 1024); } while (0)
; #define PG8_LDB(dst, b, h) do { _Pragma("unroll") for (int n = 0; n < 2; ++n) _Pragma("unroll") for (int k = 0; k < 2; ++k) dst[n][k] = *(const LAS bf16x8*)(lds + PG8_SB(b, h) + boff + n * 2048 + k * 1024); } while (0)
; #define PG8_WAIT_V(n) asm volatile("s_waitcnt vmcnt(" #n ")" ::: "memory")
; #define PG8_WAIT_L(n) asm volatile("s_waitcnt lgkmcnt(" #n ")" ::: "memory")
; #define PG8_BAR __builtin_amdgcn_s_barrier()
; #define PG8_SCHED __builtin_amdgcn_sched_barrier(0)
;     ...
;             if constexpr (SP2) {
;             PG8_LDB(B0, 0, 0); PG8_LDB(B1, 0, 1); PG8_SCHED; PG8_LDA(At, 0, 0); PG8_STAGE(PG8_SA(1, 1), a1 + ah, VA1);
;             PG8_WAIT_V(8); PG8_WAIT_L(0); PG8_BAR; PG8_MMA(0, 0, At, B0); PG8_MMA(0, 1, At, B1); PG8_BAR; PG8_SCHED;
;             PG8_LDA(At, 0, 1); PG8_STAGE(PG8_SB(0, 0), b2, voffB); PG8_STAGE(PG8_SB(0, 1), b2 + bstep, voffB); PG8_STAGE(PG8_SA(0, 0), a2, v2[0]);
;             PG8_WAIT_V(8); PG8_WAIT_L(0); PG8_BAR; if (full) { PG8_MMA(1, 0, At, B0); PG8_MMA(1, 1, At, B1); } PG8_BAR; PG8_SCHED;
.Lkr_b:
	s_cmp_eq_u32 s64, 4
	s_cselect_b32 s35, s23, s31
	s_cselect_b32 s34, s55, s30
	s_cselect_b32 s31, s19, s59
	s_cselect_b32 s30, s56, s58
	v_lshl_add_u64 v[218:219], s[28:29], 0, v[170:171]
	s_add_i32 m0, s17, 0xc000
	ds_read_b128 v[178:181], v192
	ds_read_b128 v[182:185], v192 offset:1024
	ds_read_b128 v[194:197], v192 offset:2048
	ds_read_b128 v[198:201], v192 offset:3072
	ds_read_b128 v[202:205], v192 offset:4096
	ds_read_b128 v[206:209], v192 offset:5120
	ds_read_b128 v[210:213], v192 offset:6144
	ds_read_b128 v[214:217], v192 offset:7168
	global_load_lds_dwordx4 v[218:219], off
	v_lshl_add_u64 v[218:219], s[28:29], 0, v[172:173]
	s_add_i32 m0, s17, 0xe000
	s_nop 0
	global_load_lds_dwordx4 v[218:219], off
	s_waitcnt vmcnt(8)
	s_waitcnt lgkmcnt(0)
	s_barrier
	s_setprio 1
	s_waitcnt lgkmcnt(0)
	v_mfma_scale_f32_16x16x128_f8f6f4 v[158:161], v[26:33], v[178:185], v[158:161], v1, v186 op_sel_hi:[0,0,0]
	v_mfma_scale_f32_16x16x128_f8f6f4 v[154:157], v[18:25], v[178:185], v[154:157], v1, v186 op_sel_hi:[0,0,0]
	v_mfma_scale_f32_16x16x128_f8f6f4 v[150:153], v[26:33], v[194:201], v[150:153], v1, v186 op_sel_hi:[0,0,0]
	v_mfma_scale_f32_16x16x128_f8f6f4 v[146:149], v[18:25], v[194:201], v[146:149], v1, v186 op_sel_hi:[0,0,0]
	v_mfma_scale_f32_16x16x128_f8f6f4 v[134:137], v[26:33], v[202:209], v[134:137], v1, v186 op_sel_hi:[0,0,0]
	v_mfma_scale_f32_16x16x128_f8f6f4 v[130:133], v[18:25], v[202:209], v[130:133], v1, v186 op_sel_hi:[0,0,0]
	v_mfma_scale_f32_16x16x128_f8f6f4 v[118:121], v[26:33], v[210:217], v[118:121], v1, v186 op_sel_hi:[0,0,0]
	v_mfma_scale_f32_16x16x128_f8f6f4 v[106:109], v[18:25], v[210:217], v[106:109], v1, v186 op_sel_hi:[0,0,0]
	s_setprio 0
	s_setprio 1
	v_mfma_scale_f32_16x16x128_f8f6f4 v[142:145], v[10:17], v[178:185], v[142:145], v1, v186 op_sel_hi:[0,0,0]
	v_mfma_scale_f32_16x16x128_f8f6f4 v[138:141], v[2:9], v[178:185], v[138:141], v1, v186 op_sel_hi:[0,0,0]
	v_mfma_scale_f32_16x16x128_f8f6f4 v[126:129], v[10:17], v[194:201], v[126:129], v1, v186 op_sel_hi:[0,0,0]
	v_mfma_scale_f32_16x16x128_f8f6f4 v[122:125], v[2:9], v[194:201], v[122:125], v1, v186 op_sel_hi:[0,0,0]
	v_mfma_scale_f32_16x16x128_f8f6f4 v[102:105], v[10:17], v[202:209], v[102:105], v1, v186 op_sel_hi:[0,0,0]
	v_mfma_scale_f32_16x16x128_f8f6f4 v[90:93], v[2:9], v[202:209], v[90:93], v1, v186 op_sel_hi:[0,0,0]
	v_mfma_scale_f32_16x16x128_f8f6f4 v[74:77], v[10:17], v[210:217], v[74:77], v1, v186 op_sel_hi:[0,0,0]
	v_mfma_scale_f32_16x16x128_f8f6f4 v[66:69], v[2:9], v[210:217], v[66:69], v1, v186 op_sel_hi:[0,0,0]
	s_setprio 0
	s_barrier
	s_add_i32 s65, s51, s42
	v_lshl_add_u64 v[178:179], s[30:31], 0, v[164:165]
	s_mov_b32 m0, s65
	ds_read_b128 v[194:197], v192 offset:16384
	ds_read_b128 v[198:201], v192 offset:17408
	ds_read_b128 v[202:205], v192 offset:18432
	ds_read_b128 v[206:209], v192 offset:19456
	ds_read_b128 v[210:213], v192 offset:20480
	ds_read_b128 v[214:217], v192 offset:21504
	ds_read_b128 v[218:221], v192 offset:22528
	ds_read_b128 v[222:225], v192 offset:23552
	global_load_lds_dwordx4 v[178:179], off
	s_add_i32 m0, s65, 0x2000
	s_add_u32 s66, s30, 0x20000
	v_lshl_add_u64 v[180:181], s[30:31], 0, v[162:163]
	s_addc_u32 s67, s31, 0
	s_add_i32 s65, s52, s42
	global_load_lds_dwordx4 v[180:181], off
	v_lshl_add_u64 v[182:183], s[66:67], 0, v[164:165]
	s_mov_b32 m0, s65
	v_lshl_add_u64 v[184:185], s[34:35], 0, v[168:169]
	global_load_lds_dwordx4 v[182:183], off
	v_lshl_add_u64 v[182:183], s[66:67], 0, v[162:163]
	s_add_i32 m0, s65, 0x2000
	s_nop 0
	global_load_lds_dwordx4 v[182:183], off
	v_lshl_add_u64 v[182:183], s[34:35], 0, v[166:167]
	s_mov_b32 m0, s17
	s_nop 0
	global_load_lds_dwordx4 v[182:183], off
	s_mov_b32 m0, s44
	s_nop 0
	global_load_lds_dwordx4 v[184:185], off
	s_waitcnt vmcnt(8)
	s_waitcnt lgkmcnt(0)
	s_barrier
	s_setprio 1
	s_waitcnt lgkmcnt(0)
	v_mfma_scale_f32_16x16x128_f8f6f4 v[62:65], v[26:33], v[194:201], v[62:65], v1, v186 op_sel_hi:[0,0,0]
	v_mfma_scale_f32_16x16x128_f8f6f4 v[58:61], v[18:25], v[194:201], v[58:61], v1, v186 op_sel_hi:[0,0,0]
	v_mfma_scale_f32_16x16x128_f8f6f4 v[54:57], v[26:33], v[202:209], v[54:57], v1, v186 op_sel_hi:[0,0,0]
	v_mfma_scale_f32_16x16x128_f8f6f4 v[50:53], v[18:25], v[202:209], v[50:53], v1, v186 op_sel_hi:[0,0,0]
	v_mfma_scale_f32_16x16x128_f8f6f4 v[46:49], v[26:33], v[210:217], v[46:49], v1, v186 op_sel_hi:[0,0,0]
	v_mfma_scale_f32_16x16x128_f8f6f4 v[42:45], v[18:25], v[210:217], v[42:45], v1, v186 op_sel_hi:[0,0,0]
	v_mfma_scale_f32_16x16x128_f8f6f4 v[38:41], v[26:33], v[218:225], v[38:41], v1, v186 op_sel_hi:[0,0,0]
	v_mfma_scale_f32_16x16x128_f8f6f4 v[34:37], v[18:25], v[218:225], v[34:37], v1, v186 op_sel_hi:[0,0,0]
	s_setprio 0
	s_setprio 1
	v_mfma_scale_f32_16x16x128_f8f6f4 v[110:113], v[10:17], v[194:201], v[110:113], v1, v186 op_sel_hi:[0,0,0]
	v_mfma_scale_f32_16x16x128_f8f6f4 v[114:117], v[2:9], v[194:201], v[114:117], v1, v186 op_sel_hi:[0,0,0]
	v_mfma_scale_f32_16x16x128_f8f6f4 v[94:97], v[10:17], v[202:209], v[94:97], v1, v186 op_sel_hi:[0,0,0]
	v_mfma_scale_f32_16x16x128_f8f6f4 v[98:101], v[2:9], v[202:209], v[98:101], v1, v186 op_sel_hi:[0,0,0]
	v_mfma_scale_f32_16x16x128_f8f6f4 v[82:85], v[10:17], v[210:217], v[82:85], v1, v186 op_sel_hi:[0,0,0]
	v_mfma_scale_f32_16x16x128_f8f6f4 v[86:89], v[2:9], v[210:217], v[86:89], v1, v186 op_sel_hi:[0,0,0]
	v_mfma_scale_f32_16x16x128_f8f6f4 v[70:73], v[10:17], v[218:225], v[70:73], v1, v186 op_sel_hi:[0,0,0]
	v_mfma_scale_f32_16x16x128_f8f6f4 v[78:81], v[2:9], v[218:225], v[78:81], v1, v186 op_sel_hi:[0,0,0]
	s_setprio 0
	s_barrier
; #define PG8_STAGE(bufoff, gbase, voff) do { _Pragma("unroll") for (int _i = 0; _i < 2; ++_i) \
;         __builtin_amdgcn_global_load_lds((const unsigned*)((const char*)(gbase) + (voff)[_i]), (LAS unsigned*)(lds + (bufoff) + ldsw + _i * 8192), 16, 0, 0); } while (0)
; #define PG8_LDA(dst, b, h) do { _Pragma("unroll") for (int m = 0; m < 4; ++m) _Pragma("unroll") for (int k = 0; k < 2; ++k) dst[m][k] = *(const LAS bf16x8*)(lds + PG8_SA(b, h) + aoff + m * 2048 + k * 1024); } while (0)
; #define PG8_LDB(dst, b, h) do { _Pragma("unroll") for (int n = 0; n < 2; ++n) _Pragma("unroll") for (int k = 0; k < 2; ++k) dst[n][k] = *(const LAS bf16x8*)(lds + PG8_SB(b, h) + boff + n * 2048 + k * 1024); } while (0)
; #define PG8_WAIT_V(n) asm volatile("s_waitcnt vmcnt(" #n ")" ::: "memory")
; #define PG8_WAIT_L(n) asm volatile("s_waitcnt lgkmcnt(" #n ")" ::: "memory")
; #define PG8_BAR __builtin_amdgcn_s_barrier()
; #define PG8_SCHED __builtin_amdgcn_sched_barrier(0)
;     ...
;         for (int t = 0; t < nt; t += 2) {
;             const bool last = (t == nt - 2);
;             const char* a1 = cA + (size_t)(t + 1) * kstep;
;             const char* a2 = last ? nA : cA + (size_t)(t + 2) * kstep; const char* b2 = last ? nB : cB + (size_t)(t + 2) * kstep;
;             const char* a3 = a2 + kstep; const char* b3 = b2 + kstep;
;     ...
;             PG8_LDB(B0, 1, 0); PG8_LDB(B1, 1, 1); PG8_SCHED; PG8_LDA(At, 1, 0); PG8_STAGE(PG8_SA(0, 1), a2 + ah, v2[1]);
;             PG8_WAIT_V(8); PG8_WAIT_L(0); PG8_BAR; PG8_MMA(0, 0, At, B0); PG8_MMA(0, 1, At, B1); PG8_BAR; PG8_SCHED;
;             PG8_LDA(At, 1, 1); PG8_STAGE(PG8_SB(1, 0), b3, voffB); PG8_STAGE(PG8_SB(1, 1), b3 + bstep, voffB); PG8_STAGE(PG8_SA(1, 0), a3, v2[0]);
;             PG8_WAIT_V(8); PG8_WAIT_L(0); PG8_BAR; if (full) { PG8_MMA(1, 0, At, B0); PG8_MMA(1, 1, At, B1); } PG8_BAR; PG8_SCHED;
	s_add_i32 s65, 0, 0x18000
	s_add_i32 s66, 0, 0x1c000
	v_add_u32_e32 v14, s65, v188
	v_add_u32_e32 v30, s66, v188
	ds_read_b128 v[2:5], v14
	ds_read_b128 v[6:9], v14 offset:1024
	ds_read_b128 v[10:13], v14 offset:2048
	ds_read_b128 v[14:17], v14 offset:3072
	ds_read_b128 v[18:21], v30
	ds_read_b128 v[22:25], v30 offset:1024
	ds_read_b128 v[26:29], v30 offset:2048
	ds_read_b128 v[30:33], v30 offset:3072
	s_add_u32 s34, s34, 0x20000
	s_addc_u32 s35, s35, 0
	s_mov_b32 m0, s45
	v_lshl_add_u64 v[226:227], s[34:35], 0, v[166:167]
	ds_read_b128 v[194:197], v192 offset:32768
	ds_read_b128 v[198:201], v192 offset:33792
	ds_read_b128 v[202:205], v192 offset:34816
	ds_read_b128 v[206:209], v192 offset:35840
	ds_read_b128 v[210:213], v192 offset:36864
	ds_read_b128 v[214:217], v192 offset:37888
	ds_read_b128 v[218:221], v192 offset:38912
	ds_read_b128 v[222:225], v192 offset:39936
	global_load_lds_dwordx4 v[226:227], off
	v_lshl_add_u64 v[226:227], s[34:35], 0, v[168:169]
	s_mov_b32 m0, s46
	s_nop 0
	global_load_lds_dwordx4 v[226:227], off
	s_waitcnt vmcnt(8)
	s_waitcnt lgkmcnt(0)
	s_barrier
	s_setprio 1
	s_waitcnt lgkmcnt(0)
	v_mfma_scale_f32_16x16x128_f8f6f4 v[158:161], v[2:9], v[194:201], v[158:161], v1, v186 op_sel_hi:[0,0,0]
	v_mfma_scale_f32_16x16x128_f8f6f4 v[154:157], v[10:17], v[194:201], v[154:157], v1, v186 op_sel_hi:[0,0,0]
	v_mfma_scale_f32_16x16x128_f8f6f4 v[150:153], v[2:9], v[202:209], v[150:153], v1, v186 op_sel_hi:[0,0,0]
	v_mfma_scale_f32_16x16x128_f8f6f4 v[146:149], v[10:17], v[202:209], v[146:149], v1, v186 op_sel_hi:[0,0,0]
	v_mfma_scale_f32_16x16x128_f8f6f4 v[134:137], v[2:9], v[210:217], v[134:137], v1, v186 op_sel_hi:[0,0,0]
	v_mfma_scale_f32_16x16x128_f8f6f4 v[130:133], v[10:17], v[210:217], v[130:133], v1, v186 op_sel_hi:[0,0,0]
	v_mfma_scale_f32_16x16x128_f8f6f4 v[118:121], v[2:9], v[218:225], v[118:121], v1, v186 op_sel_hi:[0,0,0]
	v_mfma_scale_f32_16x16x128_f8f6f4 v[106:109], v[10:17], v[218:225], v[106:109], v1, v186 op_sel_hi:[0,0,0]
	s_setprio 0
	s_setprio 1
	v_mfma_scale_f32_16x16x128_f8f6f4 v[142:145], v[18:25], v[194:201], v[142:145], v1, v186 op_sel_hi:[0,0,0]
	v_mfma_scale_f32_16x16x128_f8f6f4 v[138:141], v[26:33], v[194:201], v[138:141], v1, v186 op_sel_hi:[0,0,0]
	v_mfma_scale_f32_16x16x128_f8f6f4 v[126:129], v[18:25], v[202:209], v[126:129], v1, v186 op_sel_hi:[0,0,0]
	v_mfma_scale_f32_16x16x128_f8f6f4 v[122:125], v[26:33], v[202:209], v[122:125], v1, v186 op_sel_hi:[0,0,0]
	v_mfma_scale_f32_16x16x128_f8f6f4 v[102:105], v[18:25], v[210:217], v[102:105], v1, v186 op_sel_hi:[0,0,0]
	v_mfma_scale_f32_16x16x128_f8f6f4 v[90:93], v[26:33], v[210:217], v[90:93], v1, v186 op_sel_hi:[0,0,0]
	v_mfma_scale_f32_16x16x128_f8f6f4 v[74:77], v[18:25], v[218:225], v[74:77], v1, v186 op_sel_hi:[0,0,0]
	v_mfma_scale_f32_16x16x128_f8f6f4 v[66:69], v[26:33], v[218:225], v[66:69], v1, v186 op_sel_hi:[0,0,0]
	s_setprio 0
	s_barrier
	s_add_i32 s34, s65, s42
	v_lshl_add_u64 v[178:179], v[178:179], 0, s[12:13]
	s_mov_b32 m0, s34
	ds_read_b128 v[194:197], v192 offset:49152
	ds_read_b128 v[198:201], v192 offset:50176
	ds_read_b128 v[202:205], v192 offset:51200
	ds_read_b128 v[206:209], v192 offset:52224
	ds_read_b128 v[210:213], v192 offset:53248
	ds_read_b128 v[214:217], v192 offset:54272
	ds_read_b128 v[218:221], v192 offset:55296
	ds_read_b128 v[222:225], v192 offset:56320
	global_load_lds_dwordx4 v[178:179], off
	s_add_i32 m0, s34, 0x2000
	s_add_u32 s30, s30, 0x20080
	v_lshl_add_u64 v[178:179], v[180:181], 0, s[12:13]
	s_addc_u32 s31, s31, 0
	s_add_i32 s34, s66, s42
	global_load_lds_dwordx4 v[178:179], off
	v_lshl_add_u64 v[178:179], s[30:31], 0, v[164:165]
	s_mov_b32 m0, s34
	s_nop 0
	global_load_lds_dwordx4 v[178:179], off
	v_lshl_add_u64 v[178:179], s[30:31], 0, v[162:163]
	s_add_i32 m0, s34, 0x2000
	s_nop 0
	global_load_lds_dwordx4 v[178:179], off
	v_lshl_add_u64 v[178:179], v[182:183], 0, s[12:13]
	s_mov_b32 m0, s48
	s_nop 0
	global_load_lds_dwordx4 v[178:179], off
	v_lshl_add_u64 v[178:179], v[184:185], 0, s[12:13]
	s_mov_b32 m0, s49
	s_nop 0
	global_load_lds_dwordx4 v[178:179], off
	s_waitcnt vmcnt(8)
	s_waitcnt lgkmcnt(0)
	s_barrier
	s_setprio 1
	s_waitcnt lgkmcnt(0)
	v_mfma_scale_f32_16x16x128_f8f6f4 v[62:65], v[2:9], v[194:201], v[62:65], v1, v186 op_sel_hi:[0,0,0]
	v_mfma_scale_f32_16x16x128_f8f6f4 v[58:61], v[10:17], v[194:201], v[58:61], v1, v186 op_sel_hi:[0,0,0]
	v_mfma_scale_f32_16x16x128_f8f6f4 v[54:57], v[2:9], v[202:209], v[54:57], v1, v186 op_sel_hi:[0,0,0]
	v_mfma_scale_f32_16x16x128_f8f6f4 v[50:53], v[10:17], v[202:209], v[50:53], v1, v186 op_sel_hi:[0,0,0]
	v_mfma_scale_f32_16x16x128_f8f6f4 v[46:49], v[2:9], v[210:217], v[46:49], v1, v186 op_sel_hi:[0,0,0]
	v_mfma_scale_f32_16x16x128_f8f6f4 v[42:45], v[10:17], v[210:217], v[42:45], v1, v186 op_sel_hi:[0,0,0]
	v_mfma_scale_f32_16x16x128_f8f6f4 v[38:41], v[2:9], v[218:225], v[38:41], v1, v186 op_sel_hi:[0,0,0]
	v_mfma_scale_f32_16x16x128_f8f6f4 v[34:37], v[10:17], v[218:225], v[34:37], v1, v186 op_sel_hi:[0,0,0]
	s_setprio 0
	s_setprio 1
	v_mfma_scale_f32_16x16x128_f8f6f4 v[110:113], v[18:25], v[194:201], v[110:113], v1, v186 op_sel_hi:[0,0,0]
	v_mfma_scale_f32_16x16x128_f8f6f4 v[114:117], v[26:33], v[194:201], v[114:117], v1, v186 op_sel_hi:[0,0,0]
	v_mfma_scale_f32_16x16x128_f8f6f4 v[94:97], v[18:25], v[202:209], v[94:97], v1, v186 op_sel_hi:[0,0,0]
	v_mfma_scale_f32_16x16x128_f8f6f4 v[98:101], v[26:33], v[202:209], v[98:101], v1, v186 op_sel_hi:[0,0,0]
	v_mfma_scale_f32_16x16x128_f8f6f4 v[82:85], v[18:25], v[210:217], v[82:85], v1, v186 op_sel_hi:[0,0,0]
	v_mfma_scale_f32_16x16x128_f8f6f4 v[86:89], v[26:33], v[210:217], v[86:89], v1, v186 op_sel_hi:[0,0,0]
	v_mfma_scale_f32_16x16x128_f8f6f4 v[70:73], v[18:25], v[218:225], v[70:73], v1, v186 op_sel_hi:[0,0,0]
	v_mfma_scale_f32_16x16x128_f8f6f4 v[78:81], v[26:33], v[218:225], v[78:81], v1, v186 op_sel_hi:[0,0,0]
	s_setprio 0
	s_barrier
	s_cmp_eq_u32 s64, s99
	s_cbranch_scc0 .Lkr_c
	s_sub_u32 s28, s28, 0x400
	s_subb_u32 s29, s29, 0
.Lkr_c:
	s_add_i32 s64, s64, 2
	s_add_u32 s28, s28, 0x100
	s_addc_u32 s29, s29, 0
	s_add_u32 s58, s58, 0x100
	s_addc_u32 s59, s59, 0
	s_cmp_eq_u32 s64, s99
	s_cbranch_scc0 .Lkr_d
	s_sub_u32 s58, s58, 0x400
	s_subb_u32 s59, s59, 0
.Lkr_d:
	s_cmp_gt_u32 s64, 5
	s_cbranch_scc0 .LBB0_196
	s_and_b64 vcc, exec, s[14:15]
	s_cbranch_vccz .LBB0_199
	s_barrier
